# grid barrier: waiting workgroups poll the top-level release generation directly instead of the per-XCD relay word (one atomic hop less per barrier)
# baseline (speedup 1.0000x reference)
.LBB0_126:
	global_atomic_add v5, v[206:207], v1, off sc0
	v_cvt_f32_u32_e32 v3, v4
	v_sub_u32_e32 v6, 0, v4
	v_rcp_iflag_f32_e32 v3, v3
	s_nop 0
	v_mul_f32_e32 v3, 0x4f7ffffe, v3
	v_cvt_u32_f32_e32 v3, v3
	v_mul_lo_u32 v6, v6, v3
	v_mul_hi_u32 v6, v3, v6
	v_add_u32_e32 v3, v3, v6
	s_waitcnt vmcnt(0)
	v_mul_hi_u32 v3, v5, v3
	v_mul_lo_u32 v6, v3, v4
	v_sub_u32_e32 v6, v5, v6
	v_add_u32_e32 v7, 1, v3
	v_cmp_ge_u32_e32 vcc, v6, v4
	v_add_u32_e32 v5, 1, v5
	s_nop 0
	v_cndmask_b32_e32 v3, v3, v7, vcc
	v_sub_u32_e32 v7, v6, v4
	v_cndmask_b32_e32 v6, v6, v7, vcc
	v_add_u32_e32 v7, 1, v3
	v_cmp_ge_u32_e32 vcc, v6, v4
	s_nop 1
	v_cndmask_b32_e32 v3, v3, v7, vcc
	v_mul_lo_u32 v6, v4, v3
	v_add_u32_e32 v4, v6, v4
	v_cmp_ne_u32_e32 vcc, v5, v4
	s_and_saveexec_b64 s[2:3], vcc
	s_xor_b64 s[10:11], exec, s[2:3]
	s_cbranch_execz .LBB0_140
	s_waitcnt lgkmcnt(0)
	v_readlane_b32 s98, v254, 23
	v_readlane_b32 s99, v254, 24
	s_nop 4
	global_load_dword v2, v211, s[98:99] sc1
	s_waitcnt vmcnt(0)
	v_cmp_eq_u32_e32 vcc, v2, v3
	s_and_saveexec_b64 s[24:25], vcc
	s_cbranch_execz .LBB0_139
	s_mov_b32 s2, 1
	s_mov_b64 s[34:35], 0
	s_branch .LBB0_130

.LBB0_134:
	global_load_dword v2, v211, s[98:99] sc1
	s_add_i32 s2, s2, 1
	s_mov_b64 s[42:43], -1
	s_waitcnt vmcnt(0)
	v_cmp_ne_u32_e32 vcc, v2, v3
	s_orn2_b64 s[40:41], vcc, exec
	s_branch .LBB0_129

.LBB0_246:
	global_atomic_add v5, v[206:207], v1, off sc0
	v_cvt_f32_u32_e32 v3, v4
	v_sub_u32_e32 v6, 0, v4
	v_rcp_iflag_f32_e32 v3, v3
	s_nop 0
	v_mul_f32_e32 v3, 0x4f7ffffe, v3
	v_cvt_u32_f32_e32 v3, v3
	v_mul_lo_u32 v6, v6, v3
	v_mul_hi_u32 v6, v3, v6
	v_add_u32_e32 v3, v3, v6
	s_waitcnt vmcnt(0)
	v_mul_hi_u32 v3, v5, v3
	v_mul_lo_u32 v6, v3, v4
	v_sub_u32_e32 v6, v5, v6
	v_add_u32_e32 v7, 1, v3
	v_cmp_ge_u32_e32 vcc, v6, v4
	v_add_u32_e32 v5, 1, v5
	s_nop 0
	v_cndmask_b32_e32 v3, v3, v7, vcc
	v_sub_u32_e32 v7, v6, v4
	v_cndmask_b32_e32 v6, v6, v7, vcc
	v_add_u32_e32 v7, 1, v3
	v_cmp_ge_u32_e32 vcc, v6, v4
	s_nop 1
	v_cndmask_b32_e32 v3, v3, v7, vcc
	v_mul_lo_u32 v6, v4, v3
	v_add_u32_e32 v4, v6, v4
	v_cmp_ne_u32_e32 vcc, v5, v4
	s_and_saveexec_b64 s[2:3], vcc
	s_xor_b64 s[10:11], exec, s[2:3]
	s_cbranch_execz .LBB0_260
	s_waitcnt lgkmcnt(0)
	v_readlane_b32 s98, v254, 23
	v_readlane_b32 s99, v254, 24
	s_nop 4
	global_load_dword v2, v211, s[98:99] sc1
	s_waitcnt vmcnt(0)
	v_cmp_eq_u32_e32 vcc, v2, v3
	s_and_saveexec_b64 s[34:35], vcc
	s_cbranch_execz .LBB0_259
	s_mov_b32 s2, 1
	s_mov_b64 s[38:39], 0
	s_branch .LBB0_250

.LBB0_254:
	global_load_dword v2, v211, s[98:99] sc1
	s_add_i32 s2, s2, 1
	s_mov_b64 s[50:51], -1
	s_waitcnt vmcnt(0)
	v_cmp_ne_u32_e32 vcc, v2, v3
	s_orn2_b64 s[42:43], vcc, exec
	s_branch .LBB0_249

.LBB0_378:
	global_atomic_add v5, v[206:207], v1, off sc0
	v_cvt_f32_u32_e32 v3, v4
	v_sub_u32_e32 v6, 0, v4
	v_rcp_iflag_f32_e32 v3, v3
	s_nop 0
	v_mul_f32_e32 v3, 0x4f7ffffe, v3
	v_cvt_u32_f32_e32 v3, v3
	v_mul_lo_u32 v6, v6, v3
	v_mul_hi_u32 v6, v3, v6
	v_add_u32_e32 v3, v3, v6
	s_waitcnt vmcnt(0)
	v_mul_hi_u32 v3, v5, v3
	v_mul_lo_u32 v6, v3, v4
	v_sub_u32_e32 v6, v5, v6
	v_add_u32_e32 v7, 1, v3
	v_cmp_ge_u32_e32 vcc, v6, v4
	v_add_u32_e32 v5, 1, v5
	s_nop 0
	v_cndmask_b32_e32 v3, v3, v7, vcc
	v_sub_u32_e32 v7, v6, v4
	v_cndmask_b32_e32 v6, v6, v7, vcc
	v_add_u32_e32 v7, 1, v3
	v_cmp_ge_u32_e32 vcc, v6, v4
	s_nop 1
	v_cndmask_b32_e32 v3, v3, v7, vcc
	v_mul_lo_u32 v6, v4, v3
	v_add_u32_e32 v4, v6, v4
	v_cmp_ne_u32_e32 vcc, v5, v4
	s_and_saveexec_b64 s[2:3], vcc
	s_xor_b64 s[24:25], exec, s[2:3]
	s_cbranch_execz .LBB0_392
	s_waitcnt lgkmcnt(0)
	v_readlane_b32 s98, v254, 23
	v_readlane_b32 s99, v254, 24
	s_nop 4
	global_load_dword v2, v211, s[98:99] sc1
	s_waitcnt vmcnt(0)
	v_cmp_eq_u32_e32 vcc, v2, v3
	s_and_saveexec_b64 s[34:35], vcc
	s_cbranch_execz .LBB0_391
	s_mov_b32 s2, 1
	s_mov_b64 s[38:39], 0
	s_branch .LBB0_382

.LBB0_916:
	global_atomic_add v5, v[206:207], v1, off sc0
	v_cvt_f32_u32_e32 v3, v4
	v_sub_u32_e32 v6, 0, v4
	v_rcp_iflag_f32_e32 v3, v3
	s_nop 0
	v_mul_f32_e32 v3, 0x4f7ffffe, v3
	v_cvt_u32_f32_e32 v3, v3
	v_mul_lo_u32 v6, v6, v3
	v_mul_hi_u32 v6, v3, v6
	v_add_u32_e32 v3, v3, v6
	s_waitcnt vmcnt(0)
	v_mul_hi_u32 v3, v5, v3
	v_mul_lo_u32 v6, v3, v4
	v_sub_u32_e32 v6, v5, v6
	v_add_u32_e32 v7, 1, v3
	v_cmp_ge_u32_e32 vcc, v6, v4
	v_add_u32_e32 v5, 1, v5
	s_nop 0
	v_cndmask_b32_e32 v3, v3, v7, vcc
	v_sub_u32_e32 v7, v6, v4
	v_cndmask_b32_e32 v6, v6, v7, vcc
	v_add_u32_e32 v7, 1, v3
	v_cmp_ge_u32_e32 vcc, v6, v4
	s_nop 1
	v_cndmask_b32_e32 v3, v3, v7, vcc
	v_mul_lo_u32 v6, v4, v3
	v_add_u32_e32 v4, v6, v4
	v_cmp_ne_u32_e32 vcc, v5, v4
	s_and_saveexec_b64 s[2:3], vcc
	s_xor_b64 s[10:11], exec, s[2:3]
	s_cbranch_execz .LBB0_930
	s_waitcnt lgkmcnt(0)
	v_readlane_b32 s98, v254, 23
	v_readlane_b32 s99, v254, 24
	s_nop 4
	global_load_dword v2, v211, s[98:99] sc1
	s_waitcnt vmcnt(0)
	v_cmp_eq_u32_e32 vcc, v2, v3
	s_and_saveexec_b64 s[24:25], vcc
	s_cbranch_execz .LBB0_929
	s_mov_b32 s2, 1
	s_mov_b64 s[30:31], 0
	s_branch .LBB0_920

.LBB0_924:
	global_load_dword v2, v211, s[98:99] sc1
	s_add_i32 s2, s2, 1
	s_mov_b64 s[40:41], -1
	s_waitcnt vmcnt(0)
	v_cmp_ne_u32_e32 vcc, v2, v3
	s_orn2_b64 s[38:39], vcc, exec
	s_branch .LBB0_919
